# conv1r, conversion quota 3 (before attention) / 5 (after attention)
# baseline (speedup 1.0000x reference)
; __device__ __forceinline__ unsigned xb_ld(unsigned* p)              { return __hip_atomic_load(p, __ATOMIC_RELAXED, __HIP_MEMORY_SCOPE_AGENT); }
; __device__ __forceinline__ unsigned xb_add(unsigned* p, unsigned v) { return __hip_atomic_fetch_add(p, v, __ATOMIC_RELAXED, __HIP_MEMORY_SCOPE_AGENT); }
;     ...
;     unsigned ahead = 0xFFFFFFFFu;
;     if (tl == 0 && max_claims > 0) { if (xb_ld(qw) < (unsigned)target) ahead = xb_add(qw, 32u); }
;     for (int nc = 0; nc < max_claims; ++nc) {
;         if (tl == 0) { st[6] = ahead; if (ahead < (unsigned)target && nc + 1 < max_claims) ahead = (ahead + 32u < (unsigned)target) ? xb_add(qw, 32u) : 0xFFFFFFFFu; }
;         __syncthreads();
.LBB0_803:
	s_and_saveexec_b64 s[0:1], s[2:3]
	s_cbranch_execz .LBB0_811
	v_readlane_b32 s14, v254, 27
	s_cmp_lt_u32 s30, 4
	v_cmp_gt_u32_e32 vcc, s25, v129
	v_mov_b32_e32 v139, s14
	s_cselect_b64 s[14:15], -1, 0
	s_and_b64 s[16:17], vcc, s[14:15]
	ds_write_b32 v139, v129
	s_and_saveexec_b64 s[14:15], s[16:17]
	s_cbranch_execz .LBB0_810
	v_cmp_gt_u32_e32 vcc, s27, v129
	v_mov_b32_e32 v129, -1
	s_and_saveexec_b64 s[16:17], vcc
	s_cbranch_execz .LBB0_809
	s_mov_b64 s[20:21], exec
	v_mbcnt_lo_u32_b32 v129, s20, 0
	v_mbcnt_hi_u32_b32 v129, s21, v129
	v_cmp_eq_u32_e32 vcc, 0, v129
	s_and_saveexec_b64 s[18:19], vcc
	s_cbranch_execz .LBB0_808
	s_bcnt1_i32_b64 s20, s[20:21]
	s_lshl_b32 s20, s20, 5
	v_mov_b32_e32 v139, s20
	global_atomic_add v139, v193, v139, s[4:5] sc0

; __device__ __forceinline__ unsigned xb_add(unsigned* p, unsigned v) { return __hip_atomic_fetch_add(p, v, __ATOMIC_RELAXED, __HIP_MEMORY_SCOPE_AGENT); }
;     __device__ __forceinline__ unsigned char* ws() const { return *(unsigned char* const __attribute__((address_space(4)))*)(p + 232); }
;     ...
;     for (int nc = 0; nc < max_claims; ++nc) {
;         if (tl == 0) { st[6] = ahead; if (ahead < (unsigned)target && nc + 1 < max_claims) ahead = (ahead + 32u < (unsigned)target) ? xb_add(qw, 32u) : 0xFFFFFFFFu; }
;         __syncthreads();
;         const unsigned base = st[6];
;         if (base < (unsigned)Q_TOTAL) {
;             const int q0 = (int)base + wave; const bool v0 = q0 < Q_TOTAL, v1 = q0 + 8 < Q_TOTAL, v2 = q0 + 16 < Q_TOTAL, v3 = q0 + 24 < Q_TOTAL;
;             float ta[64], tb[64]; CvtDesc da, db;
;             if (v0) { da = conv_expert_desc(a, ws, q0); cvt_load(da, ta, lane); }
;             if (v1) { db = conv_expert_desc(a, ws, q0 + 8); cvt_load(db, tb, lane); }
;             if (v0) cvt_finish(da, ta, scr, lane);
;             if (v2) { da = conv_expert_desc(a, ws, q0 + 16); cvt_load(da, ta, lane); }
;             if (v1) cvt_finish(db, tb, scr, lane);
;             if (v3) { db = conv_expert_desc(a, ws, q0 + 24); cvt_load(db, tb, lane); }
;             if (v2) cvt_finish(da, ta, scr, lane);
;             if (v3) cvt_finish(db, tb, scr, lane);
;         }
;         if (base >= (unsigned)target) break;
;         __syncthreads();
.LBB0_884:
	s_cmp_ge_u32 s35, s25
	s_mov_b64 s[0:1], -1
	s_cbranch_scc1 .LBB0_802
	s_add_i32 s30, s30, 1
	s_cmp_eq_u32 s30, 5
	s_cselect_b64 s[0:1], -1, 0
	s_barrier
	s_branch .LBB0_802
